# out-projection epilogue: the eight per-token scales requested together, per-row-group drains removed (on top of v21)
# baseline (speedup 1.0000x reference)
.LBB0_1602:
	v_lshl_or_b32 v148, s77, 8, v163
	v_ashrrev_i32_e32 v149, 31, v148
	v_lshlrev_b64 v[146:147], 2, v[148:149]
	v_lshl_add_u64 v[152:153], s[26:27], 0, v[146:147]
	v_lshl_add_u64 v[150:151], s[24:25], 0, v[146:147]
	global_load_dwordx4 v[168:171], v[152:153], off
	global_load_dwordx4 v[172:175], v[150:151], off
	global_load_dwordx4 v[176:179], v[150:151], off offset:16
	global_load_dwordx4 v[180:183], v[152:153], off offset:16
	global_load_dwordx4 v[184:187], v[152:153], off offset:512
	global_load_dwordx4 v[188:191], v[150:151], off offset:512
	global_load_dwordx4 v[192:195], v[150:151], off offset:528
	global_load_dwordx4 v[196:199], v[152:153], off offset:528
	v_lshl_add_u32 v152, s52, 8, v161
	v_lshl_add_u64 v[146:147], s[16:17], 0, v[146:147]
	v_ashrrev_i32_e32 v153, 31, v152
	global_load_dwordx4 v[200:203], v[146:147], off
	global_load_dwordx4 v[204:207], v[146:147], off offset:16
	global_load_dwordx4 v[208:211], v[146:147], off offset:528
	global_load_dwordx4 v[212:215], v[146:147], off offset:512
	v_lshl_add_u64 v[146:147], v[152:153], 2, s[14:15]
	global_load_dword v216, v[146:147], off
	global_load_dword v238, v[146:147], off offset:64
	global_load_dword v239, v[146:147], off offset:128
	global_load_dword v240, v[146:147], off offset:192
	global_load_dword v241, v[146:147], off offset:512
	global_load_dword v242, v[146:147], off offset:576
	global_load_dword v243, v[146:147], off offset:640
	global_load_dword v244, v[146:147], off offset:704
	v_cvt_f32_i32_e32 v219, v127
	v_cvt_f32_i32_e32 v218, v126
	v_cvt_f32_i32_e32 v221, v129
	v_cvt_f32_i32_e32 v220, v128
	v_cvt_f32_i32_e32 v223, v123
	v_cvt_f32_i32_e32 v222, v122
	v_cvt_f32_i32_e32 v225, v125
	v_cvt_f32_i32_e32 v224, v124
	v_cvt_f32_i32_e32 v227, v119
	v_cvt_f32_i32_e32 v226, v118
	v_cvt_f32_i32_e32 v233, v117
	v_cvt_f32_i32_e32 v232, v116
	v_cvt_f32_i32_e32 v229, v121
	v_cvt_f32_i32_e32 v228, v120
	v_cvt_f32_i32_e32 v231, v115
	v_cvt_f32_i32_e32 v230, v114
	v_lshlrev_b64 v[114:115], 13, v[152:153]
	v_lshlrev_b64 v[150:151], 1, v[148:149]
	v_or_b32_e32 v234, 16, v152
	v_lshl_add_u64 v[114:115], s[12:13], 0, v[114:115]
	v_ashrrev_i32_e32 v235, 31, v234
	v_lshl_add_u64 v[114:115], v[114:115], 0, v[150:151]
	v_lshl_add_u64 v[236:237], v[234:235], 2, s[14:15]
	v_cvt_f32_i32_e32 v111, v111
	v_cvt_f32_i32_e32 v110, v110
	v_cvt_f32_i32_e32 v113, v113
	v_cvt_f32_i32_e32 v112, v112
	v_cvt_f32_i32_e32 v107, v107
	v_cvt_f32_i32_e32 v106, v106
	v_cvt_f32_i32_e32 v109, v109
	v_cvt_f32_i32_e32 v108, v108
	v_cvt_f32_i32_e32 v99, v99
	v_cvt_f32_i32_e32 v98, v98
	v_cvt_f32_i32_e32 v101, v101
	v_cvt_f32_i32_e32 v100, v100
	v_cvt_f32_i32_e32 v103, v103
	v_cvt_f32_i32_e32 v102, v102
	v_cvt_f32_i32_e32 v105, v105
	v_cvt_f32_i32_e32 v104, v104
	v_cvt_f32_i32_e32 v95, v95
	v_cvt_f32_i32_e32 v94, v94
	v_cvt_f32_i32_e32 v97, v97
	v_cvt_f32_i32_e32 v96, v96
	v_cvt_f32_i32_e32 v91, v91
	v_cvt_f32_i32_e32 v90, v90
	v_cvt_f32_i32_e32 v93, v93
	v_cvt_f32_i32_e32 v92, v92
	v_cvt_f32_i32_e32 v83, v83
	v_cvt_f32_i32_e32 v82, v82
	v_cvt_f32_i32_e32 v85, v85
	v_cvt_f32_i32_e32 v84, v84
	v_cvt_f32_i32_e32 v87, v87
	v_cvt_f32_i32_e32 v86, v86
	v_cvt_f32_i32_e32 v89, v89
	v_cvt_f32_i32_e32 v88, v88
	v_cvt_f32_i32_e32 v79, v79
	v_cvt_f32_i32_e32 v78, v78
	v_cvt_f32_i32_e32 v81, v81
	v_cvt_f32_i32_e32 v80, v80
	v_cvt_f32_i32_e32 v75, v75
	v_cvt_f32_i32_e32 v74, v74
	v_cvt_f32_i32_e32 v77, v77
	v_cvt_f32_i32_e32 v76, v76
	v_cvt_f32_i32_e32 v67, v67
	v_cvt_f32_i32_e32 v66, v66
	v_cvt_f32_i32_e32 v69, v69
	v_cvt_f32_i32_e32 v68, v68
	s_waitcnt vmcnt(0)
	v_pk_add_f32 v[116:117], v[174:175], v[170:171]
	v_pk_add_f32 v[118:119], v[172:173], v[168:169]
	v_pk_add_f32 v[122:123], v[176:177], v[180:181]
	v_pk_add_f32 v[120:121], v[178:179], v[182:183]
	v_pk_add_f32 v[124:125], v[190:191], v[186:187]
	v_pk_add_f32 v[126:127], v[188:189], v[184:185]
	v_pk_add_f32 v[128:129], v[194:195], v[198:199]
	v_pk_mul_f32 v[116:117], v[116:117], v[202:203]
	v_pk_mul_f32 v[118:119], v[118:119], v[200:201]
	v_pk_mul_f32 v[122:123], v[122:123], v[204:205]
	v_pk_add_f32 v[148:149], v[192:193], v[196:197]
	v_pk_mul_f32 v[120:121], v[120:121], v[206:207]
	v_pk_mul_f32 v[168:169], v[116:117], v[216:217] op_sel_hi:[1,0]
	v_pk_mul_f32 v[170:171], v[118:119], v[216:217] op_sel_hi:[1,0]
	v_pk_mul_f32 v[174:175], v[122:123], v[216:217] op_sel_hi:[1,0]
	v_pk_mul_f32 v[124:125], v[124:125], v[214:215]
	v_pk_mul_f32 v[126:127], v[126:127], v[212:213]
	v_pk_mul_f32 v[128:129], v[128:129], v[210:211]
	v_pk_mul_f32 v[148:149], v[148:149], v[208:209]
	v_pk_mul_f32 v[172:173], v[120:121], v[216:217] op_sel_hi:[1,0]
	v_pk_mul_f32 v[184:185], v[168:169], v[220:221]
	v_pk_mul_f32 v[168:169], v[170:171], v[218:219]
	v_pk_mul_f32 v[170:171], v[174:175], v[222:223]
	v_pk_mul_f32 v[176:177], v[124:125], v[216:217] op_sel_hi:[1,0]
	v_pk_mul_f32 v[178:179], v[126:127], v[216:217] op_sel_hi:[1,0]
	v_pk_mul_f32 v[180:181], v[128:129], v[216:217] op_sel_hi:[1,0]
	v_pk_mul_f32 v[182:183], v[148:149], v[216:217] op_sel_hi:[1,0]
	v_pk_mul_f32 v[172:173], v[172:173], v[224:225]
	v_cvt_pk_bf16_f32 v168, v168, v169
	v_cvt_pk_bf16_f32 v169, v184, v185
	v_cvt_pk_bf16_f32 v170, v170, v171
	v_pk_mul_f32 v[174:175], v[176:177], v[228:229]
	v_cvt_pk_bf16_f32 v171, v172, v173
	v_pk_mul_f32 v[176:177], v[178:179], v[226:227]
	v_pk_mul_f32 v[178:179], v[180:181], v[232:233]
	v_pk_mul_f32 v[180:181], v[182:183], v[230:231]
	global_store_dwordx4 v[114:115], v[168:171], off
	v_lshlrev_b64 v[172:173], 13, v[234:235]
	v_lshl_add_u64 v[172:173], s[12:13], 0, v[172:173]
	v_cvt_pk_bf16_f32 v168, v176, v177
	v_cvt_pk_bf16_f32 v169, v174, v175
	v_cvt_pk_bf16_f32 v170, v180, v181
	v_cvt_pk_bf16_f32 v171, v178, v179
	global_store_dwordx4 v[114:115], v[168:171], off offset:256
	s_nop 1
	v_mov_b32_e32 v168, v238
	v_lshl_add_u64 v[172:173], v[172:173], 0, v[150:151]
	v_or_b32_e32 v170, 32, v152
	v_ashrrev_i32_e32 v171, 31, v170
	v_lshl_add_u64 v[174:175], v[170:171], 2, s[14:15]
	v_cvt_f32_i32_e32 v71, v71
	v_cvt_f32_i32_e32 v70, v70
	v_cvt_f32_i32_e32 v73, v73
	v_cvt_f32_i32_e32 v72, v72
	v_cvt_f32_i32_e32 v63, v63
	v_cvt_f32_i32_e32 v62, v62
	v_cvt_f32_i32_e32 v65, v65
	v_cvt_f32_i32_e32 v64, v64
	v_cvt_f32_i32_e32 v59, v59
	v_cvt_f32_i32_e32 v58, v58
	v_cvt_f32_i32_e32 v61, v61
	v_cvt_f32_i32_e32 v60, v60
	v_cvt_f32_i32_e32 v51, v51
	v_cvt_f32_i32_e32 v50, v50
	v_cvt_f32_i32_e32 v53, v53
	v_cvt_f32_i32_e32 v52, v52
	v_cvt_f32_i32_e32 v55, v55
	v_cvt_f32_i32_e32 v54, v54
	v_cvt_f32_i32_e32 v57, v57
	v_cvt_f32_i32_e32 v56, v56
	v_cvt_f32_i32_e32 v47, v47
	v_cvt_f32_i32_e32 v46, v46
	v_cvt_f32_i32_e32 v49, v49
	v_cvt_f32_i32_e32 v48, v48
	v_cvt_f32_i32_e32 v43, v43
	v_cvt_f32_i32_e32 v42, v42
	v_cvt_f32_i32_e32 v45, v45
	v_cvt_f32_i32_e32 v44, v44
	v_cvt_f32_i32_e32 v35, v35
	v_cvt_f32_i32_e32 v34, v34
	v_cvt_f32_i32_e32 v37, v37
	v_cvt_f32_i32_e32 v36, v36
	v_cvt_f32_i32_e32 v39, v39
	v_cvt_f32_i32_e32 v38, v38
	v_cvt_f32_i32_e32 v41, v41
	v_cvt_f32_i32_e32 v40, v40
	v_cvt_f32_i32_e32 v31, v31
	v_cvt_f32_i32_e32 v30, v30
	v_cvt_f32_i32_e32 v33, v33
	v_cvt_f32_i32_e32 v32, v32
	v_cvt_f32_i32_e32 v27, v27
	v_cvt_f32_i32_e32 v26, v26
	v_cvt_f32_i32_e32 v29, v29
	v_cvt_f32_i32_e32 v28, v28
	v_cvt_f32_i32_e32 v19, v19
	v_cvt_f32_i32_e32 v18, v18
	v_cvt_f32_i32_e32 v21, v21
	v_cvt_f32_i32_e32 v20, v20
	v_cvt_f32_i32_e32 v23, v23
	v_cvt_f32_i32_e32 v22, v22
	v_cvt_f32_i32_e32 v25, v25
	v_cvt_f32_i32_e32 v24, v24
	v_cvt_f32_i32_e32 v15, v15
	v_cvt_f32_i32_e32 v14, v14
	v_cvt_f32_i32_e32 v17, v17
	v_cvt_f32_i32_e32 v16, v16
	v_cvt_f32_i32_e32 v11, v11
	v_cvt_f32_i32_e32 v10, v10
	v_cvt_f32_i32_e32 v13, v13
	v_cvt_f32_i32_e32 v12, v12
	v_cvt_f32_i32_e32 v3, v3
	v_cvt_f32_i32_e32 v2, v2
	v_cvt_f32_i32_e32 v5, v5
	v_cvt_f32_i32_e32 v4, v4
	v_cvt_f32_i32_e32 v7, v7
	v_cvt_f32_i32_e32 v6, v6
	v_cvt_f32_i32_e32 v9, v9
	v_cvt_f32_i32_e32 v8, v8
	v_pk_mul_f32 v[176:177], v[116:117], v[168:169] op_sel_hi:[1,0]
	v_pk_mul_f32 v[178:179], v[118:119], v[168:169] op_sel_hi:[1,0]
	v_pk_mul_f32 v[180:181], v[120:121], v[168:169] op_sel_hi:[1,0]
	v_pk_mul_f32 v[182:183], v[122:123], v[168:169] op_sel_hi:[1,0]
	v_pk_mul_f32 v[184:185], v[124:125], v[168:169] op_sel_hi:[1,0]
	v_pk_mul_f32 v[186:187], v[126:127], v[168:169] op_sel_hi:[1,0]
	v_pk_mul_f32 v[188:189], v[128:129], v[168:169] op_sel_hi:[1,0]
	v_pk_mul_f32 v[168:169], v[148:149], v[168:169] op_sel_hi:[1,0]
	v_pk_mul_f32 v[112:113], v[176:177], v[112:113]
	v_pk_mul_f32 v[110:111], v[178:179], v[110:111]
	v_pk_mul_f32 v[108:109], v[180:181], v[108:109]
	v_pk_mul_f32 v[106:107], v[182:183], v[106:107]
	v_pk_mul_f32 v[176:177], v[188:189], v[100:101]
	v_pk_mul_f32 v[168:169], v[168:169], v[98:99]
	v_cvt_pk_bf16_f32 v98, v110, v111
	v_cvt_pk_bf16_f32 v99, v112, v113
	v_cvt_pk_bf16_f32 v100, v106, v107
	v_cvt_pk_bf16_f32 v101, v108, v109
	v_pk_mul_f32 v[104:105], v[184:185], v[104:105]
	v_pk_mul_f32 v[102:103], v[186:187], v[102:103]
	global_store_dwordx4 v[172:173], v[98:101], off
	s_nop 1
	v_cvt_pk_bf16_f32 v98, v102, v103
	v_cvt_pk_bf16_f32 v99, v104, v105
	v_cvt_pk_bf16_f32 v100, v168, v169
	v_cvt_pk_bf16_f32 v101, v176, v177
	global_store_dwordx4 v[172:173], v[98:101], off offset:256
	s_nop 1
	v_mov_b32_e32 v98, v239
	v_lshlrev_b64 v[102:103], 13, v[170:171]
	v_or_b32_e32 v100, 48, v152
	v_lshl_add_u64 v[102:103], s[12:13], 0, v[102:103]
	v_ashrrev_i32_e32 v101, 31, v100
	v_lshl_add_u64 v[102:103], v[102:103], 0, v[150:151]
	v_lshl_add_u64 v[104:105], v[100:101], 2, s[14:15]
	v_pk_mul_f32 v[106:107], v[116:117], v[98:99] op_sel_hi:[1,0]
	v_pk_mul_f32 v[108:109], v[118:119], v[98:99] op_sel_hi:[1,0]
	v_pk_mul_f32 v[110:111], v[120:121], v[98:99] op_sel_hi:[1,0]
	v_pk_mul_f32 v[112:113], v[122:123], v[98:99] op_sel_hi:[1,0]
	v_pk_mul_f32 v[152:153], v[124:125], v[98:99] op_sel_hi:[1,0]
	v_pk_mul_f32 v[168:169], v[126:127], v[98:99] op_sel_hi:[1,0]
	v_pk_mul_f32 v[170:171], v[128:129], v[98:99] op_sel_hi:[1,0]
	v_pk_mul_f32 v[98:99], v[148:149], v[98:99] op_sel_hi:[1,0]
	v_pk_mul_f32 v[96:97], v[106:107], v[96:97]
	v_pk_mul_f32 v[94:95], v[108:109], v[94:95]
	v_pk_mul_f32 v[92:93], v[110:111], v[92:93]
	v_pk_mul_f32 v[90:91], v[112:113], v[90:91]
	v_pk_mul_f32 v[106:107], v[170:171], v[84:85]
	v_pk_mul_f32 v[98:99], v[98:99], v[82:83]
	v_cvt_pk_bf16_f32 v82, v94, v95
	v_cvt_pk_bf16_f32 v83, v96, v97
	v_cvt_pk_bf16_f32 v84, v90, v91
	v_cvt_pk_bf16_f32 v85, v92, v93
	v_pk_mul_f32 v[88:89], v[152:153], v[88:89]
	v_pk_mul_f32 v[86:87], v[168:169], v[86:87]
	global_store_dwordx4 v[102:103], v[82:85], off
	s_nop 1
	v_cvt_pk_bf16_f32 v82, v86, v87
	v_cvt_pk_bf16_f32 v83, v88, v89
	v_cvt_pk_bf16_f32 v84, v98, v99
	v_cvt_pk_bf16_f32 v85, v106, v107
	global_store_dwordx4 v[102:103], v[82:85], off offset:256
	s_nop 1
	v_mov_b32_e32 v82, v240
	v_pk_mul_f32 v[86:87], v[116:117], v[82:83] op_sel_hi:[1,0]
	v_lshlrev_b64 v[84:85], 13, v[100:101]
	v_lshl_add_u64 v[84:85], s[12:13], 0, v[84:85]
	v_pk_mul_f32 v[88:89], v[118:119], v[82:83] op_sel_hi:[1,0]
	v_pk_mul_f32 v[90:91], v[120:121], v[82:83] op_sel_hi:[1,0]
	v_pk_mul_f32 v[92:93], v[122:123], v[82:83] op_sel_hi:[1,0]
	v_pk_mul_f32 v[94:95], v[124:125], v[82:83] op_sel_hi:[1,0]
	v_pk_mul_f32 v[96:97], v[126:127], v[82:83] op_sel_hi:[1,0]
	v_pk_mul_f32 v[98:99], v[128:129], v[82:83] op_sel_hi:[1,0]
	v_pk_mul_f32 v[82:83], v[148:149], v[82:83] op_sel_hi:[1,0]
	v_lshl_add_u64 v[84:85], v[84:85], 0, v[150:151]
	v_pk_mul_f32 v[80:81], v[86:87], v[80:81]
	v_pk_mul_f32 v[78:79], v[88:89], v[78:79]
	v_pk_mul_f32 v[76:77], v[90:91], v[76:77]
	v_pk_mul_f32 v[74:75], v[92:93], v[74:75]
	v_pk_mul_f32 v[86:87], v[98:99], v[68:69]
	v_pk_mul_f32 v[82:83], v[82:83], v[66:67]
	v_cvt_pk_bf16_f32 v66, v78, v79
	v_cvt_pk_bf16_f32 v67, v80, v81
	v_cvt_pk_bf16_f32 v68, v74, v75
	v_cvt_pk_bf16_f32 v69, v76, v77
	v_pk_mul_f32 v[72:73], v[94:95], v[72:73]
	v_pk_mul_f32 v[70:71], v[96:97], v[70:71]
	global_store_dwordx4 v[84:85], v[66:69], off
	s_nop 1
	v_cvt_pk_bf16_f32 v66, v70, v71
	v_cvt_pk_bf16_f32 v67, v72, v73
	v_cvt_pk_bf16_f32 v68, v82, v83
	v_cvt_pk_bf16_f32 v69, v86, v87
	global_store_dwordx4 v[84:85], v[66:69], off offset:256
	s_nop 1
	v_mov_b32_e32 v66, v241
	v_add_co_u32_e32 v70, vcc, s73, v114
	v_lshl_add_u64 v[68:69], v[114:115], 0, s[28:29]
	s_nop 0
	v_addc_co_u32_e32 v71, vcc, 0, v115, vcc
	v_pk_mul_f32 v[72:73], v[116:117], v[66:67] op_sel_hi:[1,0]
	v_pk_mul_f32 v[74:75], v[118:119], v[66:67] op_sel_hi:[1,0]
	v_pk_mul_f32 v[76:77], v[120:121], v[66:67] op_sel_hi:[1,0]
	v_pk_mul_f32 v[78:79], v[122:123], v[66:67] op_sel_hi:[1,0]
	v_pk_mul_f32 v[80:81], v[124:125], v[66:67] op_sel_hi:[1,0]
	v_pk_mul_f32 v[82:83], v[126:127], v[66:67] op_sel_hi:[1,0]
	v_pk_mul_f32 v[84:85], v[128:129], v[66:67] op_sel_hi:[1,0]
	v_pk_mul_f32 v[66:67], v[148:149], v[66:67] op_sel_hi:[1,0]
	v_pk_mul_f32 v[64:65], v[72:73], v[64:65]
	v_pk_mul_f32 v[62:63], v[74:75], v[62:63]
	v_pk_mul_f32 v[60:61], v[76:77], v[60:61]
	v_pk_mul_f32 v[58:59], v[78:79], v[58:59]
	v_pk_mul_f32 v[72:73], v[84:85], v[52:53]
	v_pk_mul_f32 v[66:67], v[66:67], v[50:51]
	v_cvt_pk_bf16_f32 v50, v62, v63
	v_cvt_pk_bf16_f32 v51, v64, v65
	v_cvt_pk_bf16_f32 v52, v58, v59
	v_cvt_pk_bf16_f32 v53, v60, v61
	v_pk_mul_f32 v[56:57], v[80:81], v[56:57]
	v_pk_mul_f32 v[54:55], v[82:83], v[54:55]
	global_store_dwordx4 v[70:71], v[50:53], off
	s_nop 1
	v_cvt_pk_bf16_f32 v50, v54, v55
	v_cvt_pk_bf16_f32 v51, v56, v57
	v_cvt_pk_bf16_f32 v52, v66, v67
	v_cvt_pk_bf16_f32 v53, v72, v73
	global_store_dwordx4 v[68:69], v[50:53], off offset:256
	s_nop 1
	v_mov_b32_e32 v50, v242
	v_add_co_u32_e32 v54, vcc, s74, v114
	v_lshl_add_u64 v[52:53], v[114:115], 0, s[30:31]
	s_nop 0
	v_addc_co_u32_e32 v55, vcc, 0, v115, vcc
	v_pk_mul_f32 v[56:57], v[116:117], v[50:51] op_sel_hi:[1,0]
	v_pk_mul_f32 v[58:59], v[118:119], v[50:51] op_sel_hi:[1,0]
	v_pk_mul_f32 v[60:61], v[120:121], v[50:51] op_sel_hi:[1,0]
	v_pk_mul_f32 v[62:63], v[122:123], v[50:51] op_sel_hi:[1,0]
	v_pk_mul_f32 v[64:65], v[124:125], v[50:51] op_sel_hi:[1,0]
	v_pk_mul_f32 v[66:67], v[126:127], v[50:51] op_sel_hi:[1,0]
	v_pk_mul_f32 v[68:69], v[128:129], v[50:51] op_sel_hi:[1,0]
	v_pk_mul_f32 v[50:51], v[148:149], v[50:51] op_sel_hi:[1,0]
	v_pk_mul_f32 v[48:49], v[56:57], v[48:49]
	v_pk_mul_f32 v[46:47], v[58:59], v[46:47]
	v_pk_mul_f32 v[44:45], v[60:61], v[44:45]
	v_pk_mul_f32 v[42:43], v[62:63], v[42:43]
	v_pk_mul_f32 v[56:57], v[68:69], v[36:37]
	v_pk_mul_f32 v[50:51], v[50:51], v[34:35]
	v_cvt_pk_bf16_f32 v34, v46, v47
	v_cvt_pk_bf16_f32 v35, v48, v49
	v_cvt_pk_bf16_f32 v36, v42, v43
	v_cvt_pk_bf16_f32 v37, v44, v45
	v_pk_mul_f32 v[40:41], v[64:65], v[40:41]
	v_pk_mul_f32 v[38:39], v[66:67], v[38:39]
	global_store_dwordx4 v[54:55], v[34:37], off
	s_nop 1
	v_cvt_pk_bf16_f32 v34, v38, v39
	v_cvt_pk_bf16_f32 v35, v40, v41
	v_cvt_pk_bf16_f32 v36, v50, v51
	v_cvt_pk_bf16_f32 v37, v56, v57
	global_store_dwordx4 v[52:53], v[34:37], off offset:256
	s_nop 1
	v_mov_b32_e32 v34, v243
	v_add_co_u32_e32 v38, vcc, s75, v114
	v_lshl_add_u64 v[36:37], v[114:115], 0, s[34:35]
	s_nop 0
	v_addc_co_u32_e32 v39, vcc, 0, v115, vcc
	s_andn2_b64 vcc, exec, s[8:9]
	v_pk_mul_f32 v[40:41], v[116:117], v[34:35] op_sel_hi:[1,0]
	v_pk_mul_f32 v[42:43], v[118:119], v[34:35] op_sel_hi:[1,0]
	v_pk_mul_f32 v[44:45], v[120:121], v[34:35] op_sel_hi:[1,0]
	v_pk_mul_f32 v[46:47], v[122:123], v[34:35] op_sel_hi:[1,0]
	v_pk_mul_f32 v[48:49], v[124:125], v[34:35] op_sel_hi:[1,0]
	v_pk_mul_f32 v[50:51], v[126:127], v[34:35] op_sel_hi:[1,0]
	v_pk_mul_f32 v[52:53], v[128:129], v[34:35] op_sel_hi:[1,0]
	v_pk_mul_f32 v[34:35], v[148:149], v[34:35] op_sel_hi:[1,0]
	v_pk_mul_f32 v[32:33], v[40:41], v[32:33]
	v_pk_mul_f32 v[30:31], v[42:43], v[30:31]
	v_pk_mul_f32 v[28:29], v[44:45], v[28:29]
	v_pk_mul_f32 v[26:27], v[46:47], v[26:27]
	v_pk_mul_f32 v[40:41], v[52:53], v[20:21]
	v_pk_mul_f32 v[34:35], v[34:35], v[18:19]
	v_cvt_pk_bf16_f32 v18, v30, v31
	v_cvt_pk_bf16_f32 v19, v32, v33
	v_cvt_pk_bf16_f32 v20, v26, v27
	v_cvt_pk_bf16_f32 v21, v28, v29
	v_pk_mul_f32 v[24:25], v[48:49], v[24:25]
	v_pk_mul_f32 v[22:23], v[50:51], v[22:23]
	global_store_dwordx4 v[38:39], v[18:21], off
	s_nop 1
	v_cvt_pk_bf16_f32 v18, v22, v23
	v_cvt_pk_bf16_f32 v19, v24, v25
	v_cvt_pk_bf16_f32 v20, v34, v35
	v_cvt_pk_bf16_f32 v21, v40, v41
	global_store_dwordx4 v[36:37], v[18:21], off offset:256
	s_nop 1
	v_mov_b32_e32 v18, v244
	v_add_co_u32_e64 v22, s[8:9], s76, v114
	v_lshl_add_u64 v[20:21], v[114:115], 0, s[36:37]
	s_nop 0
	v_addc_co_u32_e64 v23, s[8:9], 0, v115, s[8:9]
	s_mov_b64 s[8:9], -1
	v_pk_mul_f32 v[24:25], v[116:117], v[18:19] op_sel_hi:[1,0]
	v_pk_mul_f32 v[26:27], v[118:119], v[18:19] op_sel_hi:[1,0]
	v_pk_mul_f32 v[28:29], v[120:121], v[18:19] op_sel_hi:[1,0]
	v_pk_mul_f32 v[30:31], v[122:123], v[18:19] op_sel_hi:[1,0]
	v_pk_mul_f32 v[32:33], v[124:125], v[18:19] op_sel_hi:[1,0]
	v_pk_mul_f32 v[34:35], v[126:127], v[18:19] op_sel_hi:[1,0]
	v_pk_mul_f32 v[36:37], v[128:129], v[18:19] op_sel_hi:[1,0]
	v_pk_mul_f32 v[18:19], v[148:149], v[18:19] op_sel_hi:[1,0]
	v_pk_mul_f32 v[16:17], v[24:25], v[16:17]
	v_pk_mul_f32 v[14:15], v[26:27], v[14:15]
	v_pk_mul_f32 v[12:13], v[28:29], v[12:13]
	v_pk_mul_f32 v[10:11], v[30:31], v[10:11]
	v_pk_mul_f32 v[24:25], v[36:37], v[4:5]
	v_pk_mul_f32 v[18:19], v[18:19], v[2:3]
	v_cvt_pk_bf16_f32 v2, v14, v15
	v_cvt_pk_bf16_f32 v3, v16, v17
	v_cvt_pk_bf16_f32 v4, v10, v11
	v_cvt_pk_bf16_f32 v5, v12, v13
	v_pk_mul_f32 v[8:9], v[32:33], v[8:9]
	v_pk_mul_f32 v[6:7], v[34:35], v[6:7]
	global_store_dwordx4 v[22:23], v[2:5], off
	s_nop 1
	v_cvt_pk_bf16_f32 v2, v6, v7
	v_cvt_pk_bf16_f32 v3, v8, v9
	v_cvt_pk_bf16_f32 v4, v18, v19
	v_cvt_pk_bf16_f32 v5, v24, v25
	global_store_dwordx4 v[20:21], v[2:5], off offset:256
	s_cbranch_vccnz .LBB0_1591
	s_andn2_b64 vcc, exec, s[10:11]
	s_cbranch_vccnz .LBB0_1590
	s_barrier
	s_branch .LBB0_1590
